# v38 + M2: Mamba state lines scanned by workgroups 128-255 (two lines per wave), GLA lines by workgroups 0-127: two dependent batches per wave instead of three
# speedup vs baseline: 1.0042x; 1.0013x over previous
; __device__ __forceinline__ void m2_phase(KA A, int wave, int lane, int bid, int G) {
;     unsigned char* ws = A->ws; const int gw = bid * NWAVES + wave, NGW = G * NWAVES;
;     float* CSM = (float*)(ws + WS_CSM); const float* AL = (const float*)(ws + WS_ALAST);
;     for (int line = gw; line < BATCH * 2 * 8 * 64; line += NGW) {
;         const int p = line & 63, h = (line >> 6) & 7, d = (line >> 9) & 1, b = line >> 10;
;         float c0[NCH_M], c1[NCH_M], dc[NCH_M];
; #pragma unroll
;         for (int i = 0; i < NCH_M; ++i) { const int c = d == 0 ? i : (i < 2 ? 1 - i : NCH_M + 1 - i);
;             const float* cs = CSM + (((((size_t)b * NCH_M + c) * 2 + d) * 8 + h) * 64 + p) * 128;
;             c0[i] = cs[lane]; c1[i] = cs[lane + 64]; dc[i] = AL[(((size_t)b * NCH_M + c) * 2 + d) * 8 + h]; }
.LBB0_1336:
	s_andn2_b64 vcc, exec, s[0:1]
	s_cbranch_vccnz .LBB0_1398
	s_waitcnt vmcnt(0)
	v_mov_b32_e32 v2, v0
	s_mov_b32 s4, s72
	v_readfirstlane_b32 s0, v2
	s_ashr_i32 s6, s0, 6
	s_load_dwordx2 s[0:1], s[92:93], 0xf8
	s_lshl_b32 s2, s71, 3
	v_writelane_b32 v254, s22, 26
	v_and_b32_e32 v3, 63, v2
	s_add_i32 s12, s2, s6
	s_lshl_b32 vcc_lo, s4, 3
	v_writelane_b32 v255, s27, 1
	v_writelane_b32 v254, s23, 27
	s_cmpk_gt_i32 s12, 0x7ff
	v_lshlrev_b32_e32 v2, 2, v3
	v_lshlrev_b32_e32 v4, 1, v3
	s_cbranch_scc1 .LBB0_1340
	v_mov_b32_e32 v3, v130
	s_waitcnt lgkmcnt(0)
	s_add_u32 s2, s0, 0xc00000
	v_lshl_add_u64 v[6:7], s[0:1], 0, v[2:3]
	s_mov_b64 s[8:9], 0x43c00000
	v_mov_b32_e32 v5, v130
	s_addc_u32 s13, s1, 0
	v_lshl_add_u64 v[6:7], v[6:7], 0, s[8:9]
	v_lshl_add_u64 v[8:9], s[0:1], 0, v[4:5]
	s_mov_b64 s[8:9], 0x48900000
	s_lshl_b32 s5, s71, 10
	s_lshl_b32 s6, s6, 7
	v_lshl_add_u64 v[8:9], v[8:9], 0, s[8:9]
	s_add_i32 s16, s5, s6
	s_lshl_b32 s17, s4, 10
	s_sub_i32 s18, s12, 0x400
	s_sub_i32 s16, s16, 0x20000
	s_cmp_lt_i32 s18, 0
	s_cbranch_scc1 .LBB0_1340
.LBB0_1339:
	s_ashr_i32 s33, s18, 10
	s_bfe_u32 s26, s18, 0x10009
	s_mul_i32 s33, s33, 34
	s_or_b32 s8, s26, s33
	s_bfe_u32 s19, s18, 0x30006
	s_lshl_b32 s4, s26, 3
	s_ashr_i32 s9, s8, 31
	s_or_b32 s36, s4, s19
	s_lshl_b64 s[4:5], s[8:9], 4
	s_and_b32 s27, s16, 0x1f80
	s_or_b32 s4, s4, s36
	s_lshl_b32 s24, s27, 2
	s_lshl_b64 s[6:7], s[4:5], 15
	s_lshl_b64 s[4:5], s[4:5], 2
	s_add_u32 s10, s2, s4
	s_addc_u32 s11, s13, s5
	s_xor_b32 s4, s8, 1
	s_ashr_i32 s5, s4, 31
	s_lshl_b64 s[14:15], s[4:5], 4
	s_or_b32 s14, s14, s36
	s_lshl_b64 s[20:21], s[14:15], 15
	s_lshl_b64 s[14:15], s[14:15], 2
	s_add_u32 s14, s2, s14
	s_addc_u32 s15, s13, s15
	v_lshl_add_u64 v[10:11], v[6:7], 0, s[24:25]
	s_cmp_eq_u32 s26, 0
	v_lshl_add_u64 v[14:15], v[10:11], 0, s[6:7]
	global_load_dword v13, v[14:15], off
	global_load_dword v12, v[14:15], off offset:256
	s_nop 0
	global_load_dword v15, v130, s[10:11]
	s_cselect_b32 s10, 2, 33
	s_cselect_b32 s22, 3, 32
	s_cselect_b32 s28, 4, 31
	s_cselect_b32 s30, 5, 30
	s_cselect_b32 s38, 6, 29
	s_cselect_b32 s41, 7, 28
	s_cselect_b32 s43, 8, 27
	s_cselect_b32 s40, 9, 26
	s_cselect_b32 s42, 10, 25
	s_cselect_b32 s44, 11, 24
	s_cselect_b32 s46, 12, 23
	s_cselect_b32 s48, 13, 22
	s_cselect_b32 s50, 14, 21
	s_cselect_b32 s52, 15, 20
	s_cselect_b32 s54, 16, 19
	s_cselect_b32 s60, 19, 16
	s_cselect_b32 s64, 20, 15
	s_cselect_b32 s68, 21, 14
	s_cselect_b32 s70, 22, 13
	s_cselect_b32 s72, 23, 12
	s_cselect_b32 s74, 24, 11
	s_cselect_b32 s76, 25, 10
	s_cselect_b32 s78, 26, 9
	s_cselect_b32 s67, 27, 8
	s_cselect_b32 s7, 28, 7
	s_cselect_b32 s6, 29, 6
	s_cselect_b32 s66, 30, 5
	s_cselect_b32 s63, 31, 4
	s_cselect_b32 s37, 32, 3
	s_cselect_b32 s24, 33, 2
	s_add_i32 s10, s10, s33
	v_lshl_add_u64 v[16:17], v[10:11], 0, s[20:21]
	s_ashr_i32 s11, s10, 31
	global_load_dword v5, v[16:17], off
	global_load_dword v3, v[16:17], off offset:256
	global_load_dword v14, v130, s[14:15]
	s_lshl_b64 s[14:15], s[10:11], 4
	s_or_b32 s14, s14, s36
	s_lshl_b64 s[20:21], s[14:15], 15
	s_lshl_b64 s[14:15], s[14:15], 2
	s_add_u32 s14, s2, s14
	v_lshl_add_u64 v[18:19], v[10:11], 0, s[20:21]
	s_addc_u32 s15, s13, s15
	global_load_dword v17, v[18:19], off
	global_load_dword v16, v[18:19], off offset:256
	global_load_dword v24, v130, s[14:15]
	s_add_i32 s14, s22, s33
	s_ashr_i32 s15, s14, 31
	s_lshl_b64 s[20:21], s[14:15], 4
	s_or_b32 s20, s20, s36
	s_lshl_b64 s[22:23], s[20:21], 15
	s_lshl_b64 s[20:21], s[20:21], 2
	s_add_u32 s20, s2, s20
	v_lshl_add_u64 v[20:21], v[10:11], 0, s[22:23]
	s_addc_u32 s21, s13, s21
	global_load_dword v19, v[20:21], off
	global_load_dword v18, v[20:21], off offset:256
	global_load_dword v27, v130, s[20:21]
	s_add_i32 s20, s28, s33
	s_ashr_i32 s21, s20, 31
	s_lshl_b64 s[22:23], s[20:21], 4
	s_or_b32 s22, s22, s36
	s_lshl_b64 s[28:29], s[22:23], 15
	s_lshl_b64 s[22:23], s[22:23], 2
	s_add_u32 s22, s2, s22
	v_lshl_add_u64 v[22:23], v[10:11], 0, s[28:29]
	s_addc_u32 s23, s13, s23
	global_load_dword v21, v[22:23], off
	global_load_dword v20, v[22:23], off offset:256
	global_load_dword v30, v130, s[22:23]
	s_add_i32 s22, s30, s33
	s_ashr_i32 s23, s22, 31
	s_lshl_b64 s[28:29], s[22:23], 4
	s_or_b32 s28, s28, s36
	s_lshl_b64 s[30:31], s[28:29], 15
	s_lshl_b64 s[28:29], s[28:29], 2
	s_add_u32 s28, s2, s28
	v_lshl_add_u64 v[28:29], v[10:11], 0, s[30:31]
	s_addc_u32 s29, s13, s29
	global_load_dword v23, v[28:29], off
	global_load_dword v22, v[28:29], off offset:256
	global_load_dword v33, v130, s[28:29]
	s_add_i32 s28, s38, s33
	s_ashr_i32 s29, s28, 31
	s_lshl_b64 s[30:31], s[28:29], 4
	s_or_b32 s30, s30, s36
	s_lshl_b64 s[38:39], s[30:31], 15
	s_lshl_b64 s[30:31], s[30:31], 2
	s_add_u32 s30, s2, s30
	v_lshl_add_u64 v[28:29], v[10:11], 0, s[38:39]
	s_addc_u32 s31, s13, s31
	global_load_dword v26, v[28:29], off
	global_load_dword v25, v[28:29], off offset:256
	global_load_dword v36, v130, s[30:31]
	s_add_i32 s30, s41, s33
	s_ashr_i32 s31, s30, 31
	s_lshl_b64 s[38:39], s[30:31], 4
	s_or_b32 s38, s38, s36
	s_lshl_b64 s[56:57], s[38:39], 15
	s_lshl_b64 s[38:39], s[38:39], 2
	s_add_u32 s38, s2, s38
	v_lshl_add_u64 v[34:35], v[10:11], 0, s[56:57]
	s_addc_u32 s39, s13, s39
	global_load_dword v29, v[34:35], off
	global_load_dword v28, v[34:35], off offset:256
	global_load_dword v39, v130, s[38:39]
	s_add_i32 s38, s43, s33
	s_ashr_i32 s39, s38, 31
	s_lshl_b64 s[56:57], s[38:39], 4
	s_or_b32 s56, s56, s36
	s_lshl_b64 s[58:59], s[56:57], 15
	s_lshl_b64 s[56:57], s[56:57], 2
	s_add_u32 s56, s2, s56
	s_addc_u32 s57, s13, s57
	s_add_i32 s40, s40, s33
	v_lshl_add_u64 v[34:35], v[10:11], 0, s[58:59]
; __device__ __forceinline__ void m2_phase(KA A, int wave, int lane, int bid, int G) {
;     ...
; #pragma unroll
;         for (int i = 0; i < NCH_M; ++i) { const int c = d == 0 ? i : (i < 2 ? 1 - i : NCH_M + 1 - i);
;             const float* cs = CSM + (((((size_t)b * NCH_M + c) * 2 + d) * 8 + h) * 64 + p) * 128;
;             c0[i] = cs[lane]; c1[i] = cs[lane + 64]; dc[i] = AL[(((size_t)b * NCH_M + c) * 2 + d) * 8 + h]; }
	s_ashr_i32 s41, s40, 31
	global_load_dword v32, v[34:35], off
	global_load_dword v31, v[34:35], off offset:256
	global_load_dword v42, v130, s[56:57]
	s_lshl_b64 s[56:57], s[40:41], 4
	s_or_b32 s56, s56, s36
	s_lshl_b64 s[58:59], s[56:57], 15
	s_lshl_b64 s[56:57], s[56:57], 2
	s_add_u32 s56, s2, s56
	s_addc_u32 s57, s13, s57
	s_add_i32 s42, s42, s33
	v_lshl_add_u64 v[40:41], v[10:11], 0, s[58:59]
	s_ashr_i32 s43, s42, 31
	global_load_dword v35, v[40:41], off
	global_load_dword v34, v[40:41], off offset:256
	global_load_dword v45, v130, s[56:57]
	s_lshl_b64 s[56:57], s[42:43], 4
	s_or_b32 s56, s56, s36
	s_lshl_b64 s[58:59], s[56:57], 15
	s_lshl_b64 s[56:57], s[56:57], 2
	s_add_u32 s56, s2, s56
	s_addc_u32 s57, s13, s57
	s_add_i32 s44, s44, s33
	v_lshl_add_u64 v[40:41], v[10:11], 0, s[58:59]
	s_ashr_i32 s45, s44, 31
	global_load_dword v38, v[40:41], off
	global_load_dword v37, v[40:41], off offset:256
	global_load_dword v48, v130, s[56:57]
	s_lshl_b64 s[56:57], s[44:45], 4
	s_or_b32 s56, s56, s36
	s_lshl_b64 s[58:59], s[56:57], 15
	s_lshl_b64 s[56:57], s[56:57], 2
	s_add_u32 s56, s2, s56
	s_addc_u32 s57, s13, s57
	s_add_i32 s46, s46, s33
	v_lshl_add_u64 v[46:47], v[10:11], 0, s[58:59]
	s_ashr_i32 s47, s46, 31
	global_load_dword v41, v[46:47], off
	global_load_dword v40, v[46:47], off offset:256
	global_load_dword v49, v130, s[56:57]
	s_lshl_b64 s[56:57], s[46:47], 4
	s_or_b32 s56, s56, s36
	s_lshl_b64 s[58:59], s[56:57], 15
	s_lshl_b64 s[56:57], s[56:57], 2
	s_add_u32 s56, s2, s56
	s_addc_u32 s57, s13, s57
	s_add_i32 s48, s48, s33
	v_lshl_add_u64 v[46:47], v[10:11], 0, s[58:59]
	s_ashr_i32 s49, s48, 31
	global_load_dword v44, v[46:47], off
	global_load_dword v43, v[46:47], off offset:256
	global_load_dword v50, v130, s[56:57]
	s_lshl_b64 s[56:57], s[48:49], 4
	s_or_b32 s56, s56, s36
	s_lshl_b64 s[58:59], s[56:57], 15
	s_lshl_b64 s[56:57], s[56:57], 2
	s_add_u32 s56, s2, s56
	s_addc_u32 s57, s13, s57
	s_add_i32 s50, s50, s33
	v_lshl_add_u64 v[52:53], v[10:11], 0, s[58:59]
	s_ashr_i32 s51, s50, 31
	global_load_dword v47, v[52:53], off
	global_load_dword v46, v[52:53], off offset:256
	global_load_dword v59, v130, s[56:57]
	s_lshl_b64 s[56:57], s[50:51], 4
	s_or_b32 s56, s56, s36
	s_lshl_b64 s[58:59], s[56:57], 15
	s_lshl_b64 s[56:57], s[56:57], 2
	s_add_u32 s56, s2, s56
	s_addc_u32 s57, s13, s57
	s_add_i32 s52, s52, s33
	v_lshl_add_u64 v[54:55], v[10:11], 0, s[58:59]
	s_ashr_i32 s53, s52, 31
	global_load_dword v52, v[54:55], off
	global_load_dword v51, v[54:55], off offset:256
	global_load_dword v60, v130, s[56:57]
	s_lshl_b64 s[56:57], s[52:53], 4
	s_or_b32 s56, s56, s36
	s_lshl_b64 s[58:59], s[56:57], 15
	s_lshl_b64 s[56:57], s[56:57], 2
	s_add_u32 s56, s2, s56
	s_addc_u32 s57, s13, s57
	s_add_i32 s54, s54, s33
	v_lshl_add_u64 v[56:57], v[10:11], 0, s[58:59]
	s_ashr_i32 s55, s54, 31
	global_load_dword v54, v[56:57], off
	global_load_dword v53, v[56:57], off offset:256
	global_load_dword v63, v130, s[56:57]
	s_lshl_b64 s[56:57], s[54:55], 4
	s_or_b32 s56, s56, s36
	s_lshl_b64 s[58:59], s[56:57], 15
	s_lshl_b64 s[56:57], s[56:57], 2
	s_add_u32 s56, s2, s56
	v_lshl_add_u64 v[64:65], v[10:11], 0, s[58:59]
	s_addc_u32 s57, s13, s57
	global_load_dword v56, v[64:65], off
	global_load_dword v55, v[64:65], off offset:256
	global_load_dword v66, v130, s[56:57]
	s_add_i32 s56, s8, 17
	s_ashr_i32 s57, s56, 31
	s_lshl_b64 s[58:59], s[56:57], 4
	s_or_b32 s58, s58, s36
	s_lshl_b64 s[80:81], s[58:59], 15
	s_lshl_b64 s[58:59], s[58:59], 2
	s_add_u32 s58, s2, s58
	v_lshl_add_u64 v[64:65], v[10:11], 0, s[80:81]
	s_addc_u32 s59, s13, s59
	global_load_dword v58, v[64:65], off
	global_load_dword v57, v[64:65], off offset:256
	global_load_dword v69, v130, s[58:59]
	s_sub_i32 s58, s33, s26
	s_add_i32 s58, s58, 18
	s_ashr_i32 s59, s58, 31
	s_lshl_b64 s[80:81], s[58:59], 4
	s_or_b32 s80, s80, s36
	s_lshl_b64 s[84:85], s[80:81], 15
	s_lshl_b64 s[80:81], s[80:81], 2
	s_add_u32 s80, s2, s80
	s_addc_u32 s81, s13, s81
	s_add_i32 s60, s60, s33
	v_lshl_add_u64 v[64:65], v[10:11], 0, s[84:85]
	s_ashr_i32 s61, s60, 31
	global_load_dword v62, v[64:65], off
	global_load_dword v61, v[64:65], off offset:256
	global_load_dword v72, v130, s[80:81]
	s_lshl_b64 s[80:81], s[60:61], 4
	s_or_b32 s80, s80, s36
	s_lshl_b64 s[84:85], s[80:81], 15
	s_lshl_b64 s[80:81], s[80:81], 2
	s_add_u32 s80, s2, s80
	s_addc_u32 s81, s13, s81
	s_add_i32 s64, s64, s33
	v_lshl_add_u64 v[70:71], v[10:11], 0, s[84:85]
	s_ashr_i32 s65, s64, 31
	global_load_dword v65, v[70:71], off
	global_load_dword v64, v[70:71], off offset:256
	global_load_dword v73, v130, s[80:81]
	s_lshl_b64 s[80:81], s[64:65], 4
	s_or_b32 s80, s80, s36
	s_lshl_b64 s[84:85], s[80:81], 15
	s_lshl_b64 s[80:81], s[80:81], 2
	s_add_u32 s80, s2, s80
	s_addc_u32 s81, s13, s81
	s_add_i32 s68, s68, s33
	v_lshl_add_u64 v[70:71], v[10:11], 0, s[84:85]
	s_ashr_i32 s69, s68, 31
	global_load_dword v68, v[70:71], off
	global_load_dword v67, v[70:71], off offset:256
	global_load_dword v74, v130, s[80:81]
	s_lshl_b64 s[80:81], s[68:69], 4
	s_or_b32 s80, s80, s36
	s_lshl_b64 s[84:85], s[80:81], 15
	s_lshl_b64 s[80:81], s[80:81], 2
	s_add_u32 s80, s2, s80
	s_addc_u32 s81, s13, s81
	s_add_i32 s70, s70, s33
	v_lshl_add_u64 v[76:77], v[10:11], 0, s[84:85]
	s_ashr_i32 s71, s70, 31
	global_load_dword v71, v[76:77], off
	global_load_dword v70, v[76:77], off offset:256
	global_load_dword v83, v130, s[80:81]
	s_lshl_b64 s[80:81], s[70:71], 4
	s_or_b32 s80, s80, s36
	s_lshl_b64 s[84:85], s[80:81], 15
	s_lshl_b64 s[80:81], s[80:81], 2
	s_add_u32 s80, s2, s80
	s_addc_u32 s81, s13, s81
	s_add_i32 s72, s72, s33
	v_lshl_add_u64 v[78:79], v[10:11], 0, s[84:85]
; __device__ __forceinline__ unsigned f2bf(float f) { unsigned u = __builtin_bit_cast(unsigned, f); return (u + 0x7fffu + ((u >> 16) & 1u)) >> 16; }
; #define SCHED_FENCE() __builtin_amdgcn_sched_barrier(0)
; __device__ __forceinline__ void m2_phase(KA A, int wave, int lane, int bid, int G) {
;     ...
; #pragma unroll
;         for (int i = 0; i < NCH_M; ++i) { const int c = d == 0 ? i : (i < 2 ? 1 - i : NCH_M + 1 - i);
;             const float* cs = CSM + (((((size_t)b * NCH_M + c) * 2 + d) * 8 + h) * 64 + p) * 128;
;             c0[i] = cs[lane]; c1[i] = cs[lane + 64]; dc[i] = AL[(((size_t)b * NCH_M + c) * 2 + d) * 8 + h]; }
;         SCHED_FENCE();
;         float s0 = 0.f, s1 = 0.f;
; #pragma unroll
;         for (int i = 0; i < NCH_M; ++i) { const int c = d == 0 ? i : (i < 2 ? 1 - i : NCH_M + 1 - i);
;             bf16* ss = (bf16*)(ws + WS_SSM) + (((((size_t)b * NCH_M + c) * 2 + d) * 8 + h) * 64 + p) * 128;
;             ss[lane] = (unsigned short)f2bf(s0); ss[lane + 64] = (unsigned short)f2bf(s1); const float dec = __expf(dc[i]); s0 = dec * s0 + c0[i]; s1 = dec * s1 + c1[i]; }
	s_ashr_i32 s73, s72, 31
	global_load_dword v76, v[78:79], off
	global_load_dword v75, v[78:79], off offset:256
	global_load_dword v84, v130, s[80:81]
	s_lshl_b64 s[80:81], s[72:73], 4
	s_or_b32 s80, s80, s36
	s_lshl_b64 s[84:85], s[80:81], 15
	s_lshl_b64 s[80:81], s[80:81], 2
	s_add_u32 s80, s2, s80
	s_addc_u32 s81, s13, s81
	s_add_i32 s74, s74, s33
	v_lshl_add_u64 v[80:81], v[10:11], 0, s[84:85]
	s_ashr_i32 s75, s74, 31
	global_load_dword v78, v[80:81], off
	global_load_dword v77, v[80:81], off offset:256
	global_load_dword v87, v130, s[80:81]
	s_lshl_b64 s[80:81], s[74:75], 4
	s_or_b32 s80, s80, s36
	s_lshl_b64 s[84:85], s[80:81], 15
	s_lshl_b64 s[80:81], s[80:81], 2
	s_add_u32 s80, s2, s80
	s_addc_u32 s81, s13, s81
	s_add_i32 s76, s76, s33
	v_lshl_add_u64 v[88:89], v[10:11], 0, s[84:85]
	s_ashr_i32 s77, s76, 31
	global_load_dword v80, v[88:89], off
	global_load_dword v79, v[88:89], off offset:256
	global_load_dword v90, v130, s[80:81]
	s_lshl_b64 s[80:81], s[76:77], 4
	s_or_b32 s80, s80, s36
	s_lshl_b64 s[84:85], s[80:81], 15
	s_lshl_b64 s[80:81], s[80:81], 2
	s_add_u32 s80, s2, s80
	s_addc_u32 s81, s13, s81
	s_add_i32 s78, s78, s33
	v_lshl_add_u64 v[88:89], v[10:11], 0, s[84:85]
	s_ashr_i32 s79, s78, 31
	global_load_dword v82, v[88:89], off
	global_load_dword v81, v[88:89], off offset:256
	global_load_dword v93, v130, s[80:81]
	s_lshl_b64 s[80:81], s[78:79], 4
	s_or_b32 s80, s80, s36
	s_lshl_b64 s[84:85], s[80:81], 15
	s_lshl_b64 s[80:81], s[80:81], 2
	s_add_u32 s80, s2, s80
	v_lshl_add_u64 v[88:89], v[10:11], 0, s[84:85]
	s_addc_u32 s81, s13, s81
	global_load_dword v86, v[88:89], off
	global_load_dword v85, v[88:89], off offset:256
	global_load_dword v96, v130, s[80:81]
	s_add_i32 s80, s67, s33
	s_ashr_i32 s81, s80, 31
	s_lshl_b64 s[84:85], s[80:81], 4
	s_or_b32 s84, s84, s36
	s_lshl_b64 s[86:87], s[84:85], 15
	s_lshl_b64 s[84:85], s[84:85], 2
	s_add_u32 s84, s2, s84
	v_lshl_add_u64 v[94:95], v[10:11], 0, s[86:87]
	s_addc_u32 s85, s13, s85
	global_load_dword v89, v[94:95], off
	global_load_dword v88, v[94:95], off offset:256
	global_load_dword v97, v130, s[84:85]
	s_add_i32 s84, s7, s33
	s_ashr_i32 s85, s84, 31
	s_lshl_b64 s[86:87], s[84:85], 4
	s_or_b32 s86, s86, s36
	s_lshl_b64 s[88:89], s[86:87], 15
	s_lshl_b64 s[86:87], s[86:87], 2
	s_add_u32 s86, s2, s86
	s_addc_u32 s87, s13, s87
	s_add_i32 s6, s6, s33
	v_lshl_add_u64 v[94:95], v[10:11], 0, s[88:89]
	s_ashr_i32 s7, s6, 31
	global_load_dword v92, v[94:95], off
	global_load_dword v91, v[94:95], off offset:256
	global_load_dword v98, v130, s[86:87]
	s_lshl_b64 s[86:87], s[6:7], 4
	s_or_b32 s86, s86, s36
	s_lshl_b64 s[88:89], s[86:87], 15
	s_lshl_b64 s[86:87], s[86:87], 2
	s_add_u32 s86, s2, s86
	v_lshl_add_u64 v[100:101], v[10:11], 0, s[88:89]
	s_addc_u32 s87, s13, s87
	global_load_dword v95, v[100:101], off
	global_load_dword v94, v[100:101], off offset:256
	global_load_dword v103, v130, s[86:87]
	s_add_i32 s86, s66, s33
	s_ashr_i32 s87, s86, 31
	s_lshl_b64 s[66:67], s[86:87], 4
	s_or_b32 s66, s66, s36
	s_lshl_b64 s[88:89], s[66:67], 15
	s_lshl_b64 s[66:67], s[66:67], 2
	s_add_u32 s66, s2, s66
	v_lshl_add_u64 v[104:105], v[10:11], 0, s[88:89]
	s_addc_u32 s67, s13, s67
	s_add_i32 s88, s63, s33
	s_ashr_i32 s89, s88, 31
	global_load_dword v100, v[104:105], off
	global_load_dword v99, v[104:105], off offset:256
	s_nop 0
	global_load_dword v104, v130, s[66:67]
	s_lshl_b64 s[66:67], s[88:89], 4
	s_or_b32 s66, s66, s36
	s_lshl_b64 s[90:91], s[66:67], 15
	s_lshl_b64 s[66:67], s[66:67], 2
	s_add_u32 s66, s2, s66
	v_lshl_add_u64 v[106:107], v[10:11], 0, s[90:91]
	s_addc_u32 s67, s13, s67
	s_add_i32 s90, s37, s33
	s_ashr_i32 s91, s90, 31
	s_lshl_b64 s[92:93], s[90:91], 4
	s_or_b32 s92, s92, s36
	s_lshl_b64 s[36:37], s[92:93], 15
	v_lshl_add_u64 v[10:11], v[10:11], 0, s[36:37]
	s_lshl_b64 s[36:37], s[92:93], 2
	s_add_u32 s36, s2, s36
	global_load_dword v102, v[106:107], off
	global_load_dword v101, v[106:107], off offset:256
	global_load_dword v105, v130, s[66:67]
	s_nop 0
	global_load_dword v107, v[10:11], off
	global_load_dword v106, v[10:11], off offset:256
	s_addc_u32 s37, s13, s37
	global_load_dword v108, v130, s[36:37]
	s_add_i32 s92, s24, s33
	s_ashr_i32 s93, s92, 31
	s_waitcnt vmcnt(62)
	v_mul_f32_e32 v15, 0x3fb8aa3b, v15
	v_exp_f32_e32 v15, v15
	s_lshl_b32 s24, s27, 1
	v_lshl_add_u64 v[10:11], v[8:9], 0, s[24:25]
	s_lshl_b64 s[8:9], s[8:9], 18
	s_lshl_b32 s24, s26, 17
	s_lshl_b32 s19, s19, 14
	v_mul_f32_e32 v14, 0x3fb8aa3b, v14
	s_or_b32 s24, s24, s19
	v_lshl_add_u64 v[110:111], v[10:11], 0, s[8:9]
	v_exp_f32_e32 v14, v14
	v_lshl_add_u64 v[110:111], v[110:111], 0, s[24:25]
	v_fmac_f32_e32 v13, 0, v15
	s_lshl_b64 s[4:5], s[4:5], 18
	global_store_short v[110:111], v130, off
	global_store_short v[110:111], v130, off offset:128
	v_fmac_f32_e32 v12, 0, v15
	v_bfe_u32 v15, v13, 16, 1
	v_lshl_add_u64 v[110:111], v[10:11], 0, s[4:5]
	v_add3_u32 v15, v13, v15, s82
	v_lshl_add_u64 v[110:111], v[110:111], 0, s[24:25]
	global_store_short_d16_hi v[110:111], v15, off
	v_bfe_u32 v15, v12, 16, 1
	v_fmac_f32_e32 v5, v13, v14
	v_add3_u32 v15, v12, v15, s82
	v_fmac_f32_e32 v3, v12, v14
	s_lshl_b64 s[4:5], s[10:11], 18
	v_bfe_u32 v12, v5, 16, 1
	v_add3_u32 v14, v5, v12, s82
	v_lshl_add_u64 v[12:13], v[10:11], 0, s[4:5]
	v_lshl_add_u64 v[12:13], v[12:13], 0, s[24:25]
	global_store_short_d16_hi v[12:13], v14, off
	v_mul_f32_e32 v14, 0x3fb8aa3b, v24
	v_exp_f32_e32 v14, v14
	global_store_short_d16_hi v[110:111], v15, off offset:128
	v_bfe_u32 v15, v3, 16, 1
	v_add3_u32 v15, v3, v15, s82
	v_fmac_f32_e32 v17, v5, v14
	s_lshl_b64 s[4:5], s[14:15], 18
	global_store_short_d16_hi v[12:13], v15, off offset:128
; __device__ __forceinline__ unsigned f2bf(float f) { unsigned u = __builtin_bit_cast(unsigned, f); return (u + 0x7fffu + ((u >> 16) & 1u)) >> 16; }
; __device__ __forceinline__ void m2_phase(KA A, int wave, int lane, int bid, int G) {
;     ...
;         float s0 = 0.f, s1 = 0.f;
; #pragma unroll
;         for (int i = 0; i < NCH_M; ++i) { const int c = d == 0 ? i : (i < 2 ? 1 - i : NCH_M + 1 - i);
;             bf16* ss = (bf16*)(ws + WS_SSM) + (((((size_t)b * NCH_M + c) * 2 + d) * 8 + h) * 64 + p) * 128;
;             ss[lane] = (unsigned short)f2bf(s0); ss[lane + 64] = (unsigned short)f2bf(s1); const float dec = __expf(dc[i]); s0 = dec * s0 + c0[i]; s1 = dec * s1 + c1[i]; }
	v_fmac_f32_e32 v16, v3, v14
	v_bfe_u32 v3, v17, 16, 1
	v_lshl_add_u64 v[12:13], v[10:11], 0, s[4:5]
	v_add3_u32 v3, v17, v3, s82
	v_lshl_add_u64 v[12:13], v[12:13], 0, s[24:25]
	global_store_short_d16_hi v[12:13], v3, off
	v_mul_f32_e32 v3, 0x3fb8aa3b, v27
	v_exp_f32_e32 v3, v3
	v_bfe_u32 v5, v16, 16, 1
	v_add3_u32 v5, v16, v5, s82
	s_lshl_b64 s[4:5], s[20:21], 18
	v_fmac_f32_e32 v19, v17, v3
	global_store_short_d16_hi v[12:13], v5, off offset:128
	v_fmac_f32_e32 v18, v16, v3
	v_bfe_u32 v3, v19, 16, 1
	v_lshl_add_u64 v[12:13], v[10:11], 0, s[4:5]
	v_add3_u32 v3, v19, v3, s82
	v_lshl_add_u64 v[12:13], v[12:13], 0, s[24:25]
	global_store_short_d16_hi v[12:13], v3, off
	v_mul_f32_e32 v3, 0x3fb8aa3b, v30
	v_exp_f32_e32 v3, v3
	v_bfe_u32 v5, v18, 16, 1
	v_add3_u32 v5, v18, v5, s82
	s_lshl_b64 s[4:5], s[22:23], 18
	v_fmac_f32_e32 v21, v19, v3
	global_store_short_d16_hi v[12:13], v5, off offset:128
	v_fmac_f32_e32 v20, v18, v3
	v_bfe_u32 v3, v21, 16, 1
	v_lshl_add_u64 v[12:13], v[10:11], 0, s[4:5]
	v_add3_u32 v3, v21, v3, s82
	v_lshl_add_u64 v[12:13], v[12:13], 0, s[24:25]
	global_store_short_d16_hi v[12:13], v3, off
	v_mul_f32_e32 v3, 0x3fb8aa3b, v33
	v_exp_f32_e32 v3, v3
	v_bfe_u32 v5, v20, 16, 1
	v_add3_u32 v5, v20, v5, s82
	s_lshl_b64 s[4:5], s[28:29], 18
	v_fmac_f32_e32 v23, v21, v3
	global_store_short_d16_hi v[12:13], v5, off offset:128
	v_fmac_f32_e32 v22, v20, v3
	v_bfe_u32 v3, v23, 16, 1
	v_lshl_add_u64 v[12:13], v[10:11], 0, s[4:5]
	v_add3_u32 v3, v23, v3, s82
	v_lshl_add_u64 v[12:13], v[12:13], 0, s[24:25]
	global_store_short_d16_hi v[12:13], v3, off
	v_mul_f32_e32 v3, 0x3fb8aa3b, v36
	v_exp_f32_e32 v3, v3
	v_bfe_u32 v5, v22, 16, 1
	v_add3_u32 v5, v22, v5, s82
	s_lshl_b64 s[4:5], s[30:31], 18
	v_fmac_f32_e32 v26, v23, v3
	global_store_short_d16_hi v[12:13], v5, off offset:128
	v_fmac_f32_e32 v25, v22, v3
	v_bfe_u32 v3, v26, 16, 1
	v_lshl_add_u64 v[12:13], v[10:11], 0, s[4:5]
	v_add3_u32 v3, v26, v3, s82
	v_lshl_add_u64 v[12:13], v[12:13], 0, s[24:25]
	global_store_short_d16_hi v[12:13], v3, off
	v_mul_f32_e32 v3, 0x3fb8aa3b, v39
	v_exp_f32_e32 v3, v3
	v_bfe_u32 v5, v25, 16, 1
	v_add3_u32 v5, v25, v5, s82
	s_lshl_b64 s[4:5], s[38:39], 18
	v_fmac_f32_e32 v29, v26, v3
	global_store_short_d16_hi v[12:13], v5, off offset:128
	v_fmac_f32_e32 v28, v25, v3
	v_bfe_u32 v3, v29, 16, 1
	v_lshl_add_u64 v[12:13], v[10:11], 0, s[4:5]
	v_add3_u32 v3, v29, v3, s82
	v_lshl_add_u64 v[12:13], v[12:13], 0, s[24:25]
	global_store_short_d16_hi v[12:13], v3, off
	v_mul_f32_e32 v3, 0x3fb8aa3b, v42
	v_exp_f32_e32 v3, v3
	v_bfe_u32 v5, v28, 16, 1
	v_add3_u32 v5, v28, v5, s82
	s_lshl_b64 s[4:5], s[40:41], 18
	v_fmac_f32_e32 v32, v29, v3
	global_store_short_d16_hi v[12:13], v5, off offset:128
	v_fmac_f32_e32 v31, v28, v3
	v_bfe_u32 v3, v32, 16, 1
	v_lshl_add_u64 v[12:13], v[10:11], 0, s[4:5]
	v_add3_u32 v3, v32, v3, s82
	v_lshl_add_u64 v[12:13], v[12:13], 0, s[24:25]
	global_store_short_d16_hi v[12:13], v3, off
	v_mul_f32_e32 v3, 0x3fb8aa3b, v45
	v_exp_f32_e32 v3, v3
	v_bfe_u32 v5, v31, 16, 1
	v_add3_u32 v5, v31, v5, s82
	s_lshl_b64 s[4:5], s[42:43], 18
	v_fmac_f32_e32 v35, v32, v3
	global_store_short_d16_hi v[12:13], v5, off offset:128
	v_fmac_f32_e32 v34, v31, v3
	v_bfe_u32 v3, v35, 16, 1
	v_lshl_add_u64 v[12:13], v[10:11], 0, s[4:5]
	v_add3_u32 v3, v35, v3, s82
	v_lshl_add_u64 v[12:13], v[12:13], 0, s[24:25]
	global_store_short_d16_hi v[12:13], v3, off
	v_mul_f32_e32 v3, 0x3fb8aa3b, v48
	v_exp_f32_e32 v3, v3
	v_bfe_u32 v5, v34, 16, 1
	v_add3_u32 v5, v34, v5, s82
	s_lshl_b64 s[4:5], s[44:45], 18
	v_fmac_f32_e32 v38, v35, v3
	global_store_short_d16_hi v[12:13], v5, off offset:128
	v_fmac_f32_e32 v37, v34, v3
	v_bfe_u32 v3, v38, 16, 1
	v_lshl_add_u64 v[12:13], v[10:11], 0, s[4:5]
	v_add3_u32 v3, v38, v3, s82
	v_lshl_add_u64 v[12:13], v[12:13], 0, s[24:25]
	global_store_short_d16_hi v[12:13], v3, off
	v_mul_f32_e32 v3, 0x3fb8aa3b, v49
	v_exp_f32_e32 v3, v3
	v_bfe_u32 v5, v37, 16, 1
	v_add3_u32 v5, v37, v5, s82
	s_lshl_b64 s[4:5], s[46:47], 18
	v_fmac_f32_e32 v41, v38, v3
	global_store_short_d16_hi v[12:13], v5, off offset:128
	v_fmac_f32_e32 v40, v37, v3
	v_bfe_u32 v3, v41, 16, 1
	v_lshl_add_u64 v[12:13], v[10:11], 0, s[4:5]
	v_add3_u32 v3, v41, v3, s82
	v_lshl_add_u64 v[12:13], v[12:13], 0, s[24:25]
	global_store_short_d16_hi v[12:13], v3, off
	s_waitcnt vmcnt(62)
; __device__ __forceinline__ unsigned f2bf(float f) { unsigned u = __builtin_bit_cast(unsigned, f); return (u + 0x7fffu + ((u >> 16) & 1u)) >> 16; }
; __device__ __forceinline__ void m2_phase(KA A, int wave, int lane, int bid, int G) {
;     ...
;         float s0 = 0.f, s1 = 0.f;
; #pragma unroll
;         for (int i = 0; i < NCH_M; ++i) { const int c = d == 0 ? i : (i < 2 ? 1 - i : NCH_M + 1 - i);
;             bf16* ss = (bf16*)(ws + WS_SSM) + (((((size_t)b * NCH_M + c) * 2 + d) * 8 + h) * 64 + p) * 128;
;             ss[lane] = (unsigned short)f2bf(s0); ss[lane + 64] = (unsigned short)f2bf(s1); const float dec = __expf(dc[i]); s0 = dec * s0 + c0[i]; s1 = dec * s1 + c1[i]; }
	v_mul_f32_e32 v3, 0x3fb8aa3b, v50
	v_exp_f32_e32 v3, v3
	v_bfe_u32 v5, v40, 16, 1
	v_add3_u32 v5, v40, v5, s82
	s_lshl_b64 s[4:5], s[48:49], 18
	v_fmac_f32_e32 v44, v41, v3
	global_store_short_d16_hi v[12:13], v5, off offset:128
	v_fmac_f32_e32 v43, v40, v3
	v_bfe_u32 v3, v44, 16, 1
	v_lshl_add_u64 v[12:13], v[10:11], 0, s[4:5]
	v_add3_u32 v3, v44, v3, s82
	v_lshl_add_u64 v[12:13], v[12:13], 0, s[24:25]
	global_store_short_d16_hi v[12:13], v3, off
	v_mul_f32_e32 v3, 0x3fb8aa3b, v59
	v_exp_f32_e32 v3, v3
	v_bfe_u32 v5, v43, 16, 1
	v_add3_u32 v5, v43, v5, s82
	s_lshl_b64 s[4:5], s[50:51], 18
	v_fmac_f32_e32 v47, v44, v3
	global_store_short_d16_hi v[12:13], v5, off offset:128
	v_fmac_f32_e32 v46, v43, v3
	v_bfe_u32 v3, v47, 16, 1
	v_lshl_add_u64 v[12:13], v[10:11], 0, s[4:5]
	v_add3_u32 v3, v47, v3, s82
	v_lshl_add_u64 v[12:13], v[12:13], 0, s[24:25]
	global_store_short_d16_hi v[12:13], v3, off
	v_mul_f32_e32 v3, 0x3fb8aa3b, v60
	v_exp_f32_e32 v3, v3
	v_bfe_u32 v5, v46, 16, 1
	v_add3_u32 v5, v46, v5, s82
	s_lshl_b64 s[4:5], s[52:53], 18
	v_fmac_f32_e32 v52, v47, v3
	global_store_short_d16_hi v[12:13], v5, off offset:128
	v_fmac_f32_e32 v51, v46, v3
	v_bfe_u32 v3, v52, 16, 1
	v_lshl_add_u64 v[12:13], v[10:11], 0, s[4:5]
	v_add3_u32 v3, v52, v3, s82
	v_lshl_add_u64 v[12:13], v[12:13], 0, s[24:25]
	global_store_short_d16_hi v[12:13], v3, off
	v_mul_f32_e32 v3, 0x3fb8aa3b, v63
	v_exp_f32_e32 v3, v3
	v_bfe_u32 v5, v51, 16, 1
	v_add3_u32 v5, v51, v5, s82
	s_lshl_b64 s[4:5], s[54:55], 18
	v_fmac_f32_e32 v54, v52, v3
	global_store_short_d16_hi v[12:13], v5, off offset:128
	v_fmac_f32_e32 v53, v51, v3
	v_bfe_u32 v3, v54, 16, 1
	v_lshl_add_u64 v[12:13], v[10:11], 0, s[4:5]
	v_add3_u32 v3, v54, v3, s82
	v_lshl_add_u64 v[12:13], v[12:13], 0, s[24:25]
	global_store_short_d16_hi v[12:13], v3, off
	v_mul_f32_e32 v3, 0x3fb8aa3b, v66
	v_exp_f32_e32 v3, v3
	v_bfe_u32 v5, v53, 16, 1
	v_add3_u32 v5, v53, v5, s82
	s_lshl_b64 s[4:5], s[56:57], 18
	v_fmac_f32_e32 v56, v54, v3
	global_store_short_d16_hi v[12:13], v5, off offset:128
	v_fmac_f32_e32 v55, v53, v3
	v_bfe_u32 v3, v56, 16, 1
	v_lshl_add_u64 v[12:13], v[10:11], 0, s[4:5]
	v_add3_u32 v3, v56, v3, s82
	v_lshl_add_u64 v[12:13], v[12:13], 0, s[24:25]
	global_store_short_d16_hi v[12:13], v3, off
	v_mul_f32_e32 v3, 0x3fb8aa3b, v69
	v_exp_f32_e32 v3, v3
	v_bfe_u32 v5, v55, 16, 1
	v_add3_u32 v5, v55, v5, s82
	s_lshl_b64 s[4:5], s[58:59], 18
	v_fmac_f32_e32 v58, v56, v3
	global_store_short_d16_hi v[12:13], v5, off offset:128
	v_fmac_f32_e32 v57, v55, v3
	v_bfe_u32 v3, v58, 16, 1
	v_lshl_add_u64 v[12:13], v[10:11], 0, s[4:5]
	v_add3_u32 v3, v58, v3, s82
	v_lshl_add_u64 v[12:13], v[12:13], 0, s[24:25]
	global_store_short_d16_hi v[12:13], v3, off
	v_mul_f32_e32 v3, 0x3fb8aa3b, v72
	v_exp_f32_e32 v3, v3
	v_bfe_u32 v5, v57, 16, 1
	v_add3_u32 v5, v57, v5, s82
	s_lshl_b64 s[4:5], s[60:61], 18
	v_fmac_f32_e32 v62, v58, v3
	global_store_short_d16_hi v[12:13], v5, off offset:128
	v_fmac_f32_e32 v61, v57, v3
	v_bfe_u32 v3, v62, 16, 1
	v_lshl_add_u64 v[12:13], v[10:11], 0, s[4:5]
	v_add3_u32 v3, v62, v3, s82
	v_lshl_add_u64 v[12:13], v[12:13], 0, s[24:25]
	global_store_short_d16_hi v[12:13], v3, off
	v_mul_f32_e32 v3, 0x3fb8aa3b, v73
	v_exp_f32_e32 v3, v3
	v_bfe_u32 v5, v61, 16, 1
	v_add3_u32 v5, v61, v5, s82
	s_lshl_b64 s[4:5], s[64:65], 18
	v_fmac_f32_e32 v65, v62, v3
	global_store_short_d16_hi v[12:13], v5, off offset:128
	v_fmac_f32_e32 v64, v61, v3
	v_bfe_u32 v3, v65, 16, 1
	v_lshl_add_u64 v[12:13], v[10:11], 0, s[4:5]
	v_add3_u32 v3, v65, v3, s82
	v_lshl_add_u64 v[12:13], v[12:13], 0, s[24:25]
	global_store_short_d16_hi v[12:13], v3, off
	s_waitcnt vmcnt(62)
; __device__ __forceinline__ unsigned f2bf(float f) { unsigned u = __builtin_bit_cast(unsigned, f); return (u + 0x7fffu + ((u >> 16) & 1u)) >> 16; }
; #define SCHED_FENCE() __builtin_amdgcn_sched_barrier(0)
; __device__ __forceinline__ void m2_phase(KA A, int wave, int lane, int bid, int G) {
;     ...
;     for (int line = gw; line < BATCH * 2 * 8 * 64; line += NGW) {
;         const int p = line & 63, h = (line >> 6) & 7, d = (line >> 9) & 1, b = line >> 10;
;         float c0[NCH_M], c1[NCH_M], dc[NCH_M];
; #pragma unroll
;         for (int i = 0; i < NCH_M; ++i) { const int c = d == 0 ? i : (i < 2 ? 1 - i : NCH_M + 1 - i);
;             const float* cs = CSM + (((((size_t)b * NCH_M + c) * 2 + d) * 8 + h) * 64 + p) * 128;
;             c0[i] = cs[lane]; c1[i] = cs[lane + 64]; dc[i] = AL[(((size_t)b * NCH_M + c) * 2 + d) * 8 + h]; }
;         SCHED_FENCE();
;         float s0 = 0.f, s1 = 0.f;
; #pragma unroll
;         for (int i = 0; i < NCH_M; ++i) { const int c = d == 0 ? i : (i < 2 ? 1 - i : NCH_M + 1 - i);
;             bf16* ss = (bf16*)(ws + WS_SSM) + (((((size_t)b * NCH_M + c) * 2 + d) * 8 + h) * 64 + p) * 128;
;             ss[lane] = (unsigned short)f2bf(s0); ss[lane + 64] = (unsigned short)f2bf(s1); const float dec = __expf(dc[i]); s0 = dec * s0 + c0[i]; s1 = dec * s1 + c1[i]; }
	v_mul_f32_e32 v3, 0x3fb8aa3b, v74
	v_exp_f32_e32 v3, v3
	v_bfe_u32 v5, v64, 16, 1
	v_add3_u32 v5, v64, v5, s82
	s_lshl_b64 s[4:5], s[68:69], 18
	v_fmac_f32_e32 v68, v65, v3
	global_store_short_d16_hi v[12:13], v5, off offset:128
	v_fmac_f32_e32 v67, v64, v3
	v_bfe_u32 v3, v68, 16, 1
	v_lshl_add_u64 v[12:13], v[10:11], 0, s[4:5]
	v_add3_u32 v3, v68, v3, s82
	v_lshl_add_u64 v[12:13], v[12:13], 0, s[24:25]
	global_store_short_d16_hi v[12:13], v3, off
	v_mul_f32_e32 v3, 0x3fb8aa3b, v83
	v_exp_f32_e32 v3, v3
	v_bfe_u32 v5, v67, 16, 1
	v_add3_u32 v5, v67, v5, s82
	s_lshl_b64 s[4:5], s[70:71], 18
	v_fmac_f32_e32 v71, v68, v3
	global_store_short_d16_hi v[12:13], v5, off offset:128
	v_fmac_f32_e32 v70, v67, v3
	v_bfe_u32 v3, v71, 16, 1
	v_lshl_add_u64 v[12:13], v[10:11], 0, s[4:5]
	v_add3_u32 v3, v71, v3, s82
	v_lshl_add_u64 v[12:13], v[12:13], 0, s[24:25]
	global_store_short_d16_hi v[12:13], v3, off
	v_mul_f32_e32 v3, 0x3fb8aa3b, v84
	v_exp_f32_e32 v3, v3
	v_bfe_u32 v5, v70, 16, 1
	v_add3_u32 v5, v70, v5, s82
	s_lshl_b64 s[4:5], s[72:73], 18
	v_fmac_f32_e32 v76, v71, v3
	global_store_short_d16_hi v[12:13], v5, off offset:128
	v_fmac_f32_e32 v75, v70, v3
	v_bfe_u32 v3, v76, 16, 1
	v_lshl_add_u64 v[12:13], v[10:11], 0, s[4:5]
	v_add3_u32 v3, v76, v3, s82
	v_lshl_add_u64 v[12:13], v[12:13], 0, s[24:25]
	global_store_short_d16_hi v[12:13], v3, off
	v_mul_f32_e32 v3, 0x3fb8aa3b, v87
	v_exp_f32_e32 v3, v3
	v_bfe_u32 v5, v75, 16, 1
	v_add3_u32 v5, v75, v5, s82
	s_lshl_b64 s[4:5], s[74:75], 18
	v_fmac_f32_e32 v78, v76, v3
	global_store_short_d16_hi v[12:13], v5, off offset:128
	v_fmac_f32_e32 v77, v75, v3
	v_bfe_u32 v3, v78, 16, 1
	v_lshl_add_u64 v[12:13], v[10:11], 0, s[4:5]
	v_add3_u32 v3, v78, v3, s82
	v_lshl_add_u64 v[12:13], v[12:13], 0, s[24:25]
	global_store_short_d16_hi v[12:13], v3, off
	v_mul_f32_e32 v3, 0x3fb8aa3b, v90
	v_exp_f32_e32 v3, v3
	v_bfe_u32 v5, v77, 16, 1
	v_add3_u32 v5, v77, v5, s82
	s_lshl_b64 s[4:5], s[76:77], 18
	v_fmac_f32_e32 v80, v78, v3
	global_store_short_d16_hi v[12:13], v5, off offset:128
	v_fmac_f32_e32 v79, v77, v3
	v_bfe_u32 v3, v80, 16, 1
	v_lshl_add_u64 v[12:13], v[10:11], 0, s[4:5]
	v_add3_u32 v3, v80, v3, s82
	v_lshl_add_u64 v[12:13], v[12:13], 0, s[24:25]
	global_store_short_d16_hi v[12:13], v3, off
	v_mul_f32_e32 v3, 0x3fb8aa3b, v93
	v_exp_f32_e32 v3, v3
	v_bfe_u32 v5, v79, 16, 1
	v_add3_u32 v5, v79, v5, s82
	s_lshl_b64 s[4:5], s[78:79], 18
	v_fmac_f32_e32 v82, v80, v3
	global_store_short_d16_hi v[12:13], v5, off offset:128
	v_fmac_f32_e32 v81, v79, v3
	v_bfe_u32 v3, v82, 16, 1
	v_lshl_add_u64 v[12:13], v[10:11], 0, s[4:5]
	v_add3_u32 v3, v82, v3, s82
	v_lshl_add_u64 v[12:13], v[12:13], 0, s[24:25]
	global_store_short_d16_hi v[12:13], v3, off
	s_waitcnt vmcnt(62)
	v_mul_f32_e32 v3, 0x3fb8aa3b, v96
	v_exp_f32_e32 v3, v3
	v_bfe_u32 v5, v81, 16, 1
	v_add3_u32 v5, v81, v5, s82
	s_lshl_b64 s[4:5], s[80:81], 18
	v_fmac_f32_e32 v86, v82, v3
	global_store_short_d16_hi v[12:13], v5, off offset:128
	v_fmac_f32_e32 v85, v81, v3
	v_bfe_u32 v3, v86, 16, 1
	v_lshl_add_u64 v[12:13], v[10:11], 0, s[4:5]
	v_add3_u32 v3, v86, v3, s82
	v_lshl_add_u64 v[12:13], v[12:13], 0, s[24:25]
	global_store_short_d16_hi v[12:13], v3, off
	v_mul_f32_e32 v3, 0x3fb8aa3b, v97
	v_exp_f32_e32 v3, v3
	v_bfe_u32 v5, v85, 16, 1
	v_add3_u32 v5, v85, v5, s82
	s_lshl_b64 s[4:5], s[84:85], 18
	v_fmac_f32_e32 v89, v86, v3
	global_store_short_d16_hi v[12:13], v5, off offset:128
	v_fmac_f32_e32 v88, v85, v3
	v_bfe_u32 v3, v89, 16, 1
	v_lshl_add_u64 v[12:13], v[10:11], 0, s[4:5]
	v_add3_u32 v3, v89, v3, s82
	v_lshl_add_u64 v[12:13], v[12:13], 0, s[24:25]
	global_store_short_d16_hi v[12:13], v3, off
	v_mul_f32_e32 v3, 0x3fb8aa3b, v98
	v_exp_f32_e32 v3, v3
	v_bfe_u32 v5, v88, 16, 1
	v_add3_u32 v5, v88, v5, s82
	s_lshl_b64 s[4:5], s[6:7], 18
	v_fmac_f32_e32 v92, v89, v3
	global_store_short_d16_hi v[12:13], v5, off offset:128
	v_fmac_f32_e32 v91, v88, v3
	v_bfe_u32 v3, v92, 16, 1
	v_lshl_add_u64 v[12:13], v[10:11], 0, s[4:5]
	v_add3_u32 v3, v92, v3, s82
	v_lshl_add_u64 v[12:13], v[12:13], 0, s[24:25]
	global_store_short_d16_hi v[12:13], v3, off
	v_mul_f32_e32 v3, 0x3fb8aa3b, v103
	v_exp_f32_e32 v3, v3
	v_bfe_u32 v5, v91, 16, 1
	v_add3_u32 v5, v91, v5, s82
	s_lshl_b64 s[4:5], s[86:87], 18
	v_fmac_f32_e32 v95, v92, v3
	global_store_short_d16_hi v[12:13], v5, off offset:128
	v_fmac_f32_e32 v94, v91, v3
	v_bfe_u32 v3, v95, 16, 1
	v_lshl_add_u64 v[12:13], v[10:11], 0, s[4:5]
	v_add3_u32 v3, v95, v3, s82
	v_lshl_add_u64 v[12:13], v[12:13], 0, s[24:25]
	global_store_short_d16_hi v[12:13], v3, off
	s_waitcnt vmcnt(62)
	v_mul_f32_e32 v3, 0x3fb8aa3b, v104
	v_exp_f32_e32 v3, v3
	v_bfe_u32 v5, v94, 16, 1
	v_add3_u32 v5, v94, v5, s82
	s_lshl_b64 s[4:5], s[88:89], 18
	v_fmac_f32_e32 v100, v95, v3
	global_store_short_d16_hi v[12:13], v5, off offset:128
	v_fmac_f32_e32 v99, v94, v3
	v_bfe_u32 v3, v100, 16, 1
	v_lshl_add_u64 v[12:13], v[10:11], 0, s[4:5]
	v_add3_u32 v3, v100, v3, s82
	v_lshl_add_u64 v[12:13], v[12:13], 0, s[24:25]
	global_store_short_d16_hi v[12:13], v3, off
	v_mul_f32_e32 v3, 0x3fb8aa3b, v105
	v_exp_f32_e32 v3, v3
	v_bfe_u32 v5, v99, 16, 1
	v_add3_u32 v5, v99, v5, s82
	s_lshl_b64 s[4:5], s[90:91], 18
	v_fmac_f32_e32 v102, v100, v3
	global_store_short_d16_hi v[12:13], v5, off offset:128
	v_fmac_f32_e32 v101, v99, v3
	v_bfe_u32 v3, v102, 16, 1
	v_lshl_add_u64 v[12:13], v[10:11], 0, s[4:5]
	v_add3_u32 v3, v102, v3, s82
	v_lshl_add_u64 v[12:13], v[12:13], 0, s[24:25]
	global_store_short_d16_hi v[12:13], v3, off
	s_waitcnt vmcnt(62)
	v_mul_f32_e32 v3, 0x3fb8aa3b, v108
	v_exp_f32_e32 v3, v3
	s_lshl_b64 s[4:5], s[92:93], 18
	v_lshl_add_u64 v[10:11], v[10:11], 0, s[4:5]
	v_lshl_add_u64 v[10:11], v[10:11], 0, s[24:25]
	v_fmac_f32_e32 v107, v102, v3
	v_fmac_f32_e32 v106, v101, v3
	v_bfe_u32 v3, v107, 16, 1
	v_add3_u32 v3, v107, v3, s82
	v_bfe_u32 v5, v101, 16, 1
	global_store_short_d16_hi v[10:11], v3, off
	v_bfe_u32 v3, v106, 16, 1
	s_addk_i32 s18, 0x400
	s_add_i32 s16, s16, 0x20000
	v_add3_u32 v5, v101, v5, s82
	v_add3_u32 v3, v106, v3, s82
	s_cmpk_gt_i32 s18, 0x7ff
	global_store_short_d16_hi v[12:13], v5, off offset:128
	global_store_short_d16_hi v[10:11], v3, off offset:128
	s_cbranch_scc0 .LBB0_1339
